# v25: v24 with nt removed from nca1's four large output stores too (all output stores plain write-back)
# baseline (speedup 1.0000x reference)
.LBB2_38:
	s_andn2_saveexec_b64 s[0:1], s[0:1]
	s_cbranch_execz .LBB2_41
	v_and_b32_e32 v0, 3, v26
	v_mul_u32_u24_e32 v0, 0x1100, v0
	s_add_i32 s0, 0, 0x1c880
	v_mul_u32_u24_e32 v1, 0x110, v59
	v_add3_u32 v0, s0, v0, v1
	v_lshl_add_u32 v1, v39, 2, v0
	ds_write_b128 v1, v[14:17]
	ds_write_b128 v1, v[22:25] offset:64
	ds_write_b128 v1, v[10:13] offset:128
	ds_write_b128 v1, v[18:21] offset:192
	v_lshlrev_b32_e32 v1, 8, v59
	s_movk_i32 s2, 0x110
	v_sub_u32_e32 v4, v0, v1
	v_lshlrev_b32_e32 v0, 2, v27
	v_mov_b32_e32 v1, 0
	v_lshl_add_u64 v[2:3], s[64:65], 0, v[0:1]
	s_mov_b64 s[0:1], 0xa0000
	v_mad_u32_u24 v18, v50, s2, v4
	v_lshl_add_u64 v[14:15], v[2:3], 0, s[0:1]
	ds_read_b128 v[2:5], v18
	v_lshl_or_b32 v0, v58, 7, v57
	v_or3_b32 v0, v0, s28, v50
	ds_read_b128 v[10:13], v18 offset:1088
	v_lshlrev_b32_e32 v0, 6, v0
	v_lshl_add_u64 v[16:17], v[0:1], 2, v[14:15]
	s_waitcnt lgkmcnt(1)
	global_store_dwordx4 v[16:17], v[2:5], off
	v_or_b32_e32 v16, 0x4000, v0
	v_mov_b32_e32 v17, v1
	v_or_b32_e32 v2, 0x2000, v0
	v_mov_b32_e32 v3, v1
	v_lshl_add_u64 v[2:3], v[2:3], 2, v[14:15]
	s_waitcnt lgkmcnt(0)
	global_store_dwordx4 v[2:3], v[10:13], off
	ds_read_b128 v[2:5], v18 offset:2176
	ds_read_b128 v[10:13], v18 offset:3264
	v_lshl_add_u64 v[16:17], v[16:17], 2, v[14:15]
	v_or_b32_e32 v0, 0x6000, v0
	v_cmp_gt_u32_e32 vcc, 32, v38
	s_waitcnt lgkmcnt(1)
	global_store_dwordx4 v[16:17], v[2:5], off
	s_nop 1
	v_lshl_add_u64 v[2:3], v[0:1], 2, v[14:15]
	s_waitcnt lgkmcnt(0)
	global_store_dwordx4 v[2:3], v[10:13], off
	s_and_saveexec_b64 s[0:1], vcc
	s_cbranch_execz .LBB2_41
	v_lshlrev_b32_e32 v0, 3, v56
	v_lshl_add_u64 v[2:3], v[0:1], 2, s[64:65]
	v_lshlrev_b32_e32 v0, 2, v39
	v_lshl_add_u64 v[0:1], v[2:3], 0, v[0:1]
	v_add_co_u32_e32 v0, vcc, 0x4a0000, v0
	s_nop 1
	v_addc_co_u32_e32 v1, vcc, 0, v1, vcc
	global_store_dwordx4 v[0:1], v[6:9], off
